# baseline (speedup 1.0000x reference)
.LBB3_3:
	v_lshrrev_b32_e32 v2, 2, v0
	v_sub_u32_e32 v2, 0, v2
	s_lshr_b32 s9, s5, 2
	s_load_dwordx2 s[2:3], s[0:1], 0x30
	s_load_dwordx2 s[14:15], s[0:1], 0x8
	v_and_b32_e32 v34, 15, v0
	v_bitop3_b32 v2, v1, v2, 3 bitop3:0x78
	s_and_b32 s9, s9, 64
	s_lshl_b32 s10, s6, 5
	v_lshlrev_b32_e32 v35, 4, v2
	v_or_b32_e32 v2, s9, v34
	s_and_b32 s10, s10, 0x60
	v_lshlrev_b32_e32 v36, 6, v2
	v_or_b32_e32 v2, s10, v34
	v_lshlrev_b32_e32 v37, 6, v2
	v_mov_b32_e32 v2, 0
	s_mov_b32 s8, 0
	s_mov_b32 s11, 28
	v_mov_b32_e32 v3, v2
	v_mov_b32_e32 v4, v2
	v_mov_b32_e32 v5, v2
	v_mov_b32_e32 v10, v2
	v_mov_b32_e32 v11, v2
	v_mov_b32_e32 v12, v2
	v_mov_b32_e32 v13, v2
	v_mov_b32_e32 v6, v2
	v_mov_b32_e32 v7, v2
	v_mov_b32_e32 v8, v2
	v_mov_b32_e32 v9, v2
	v_mov_b32_e32 v18, v2
	v_mov_b32_e32 v19, v2
	v_mov_b32_e32 v20, v2
	v_mov_b32_e32 v21, v2
	v_mov_b32_e32 v14, v2
	v_mov_b32_e32 v15, v2
	v_mov_b32_e32 v16, v2
	v_mov_b32_e32 v17, v2
	v_mov_b32_e32 v26, v2
	v_mov_b32_e32 v27, v2
	v_mov_b32_e32 v28, v2
	v_mov_b32_e32 v29, v2
	v_mov_b32_e32 v22, v2
	v_mov_b32_e32 v23, v2
	v_mov_b32_e32 v24, v2
	v_mov_b32_e32 v25, v2
	v_mov_b32_e32 v30, v2
	v_mov_b32_e32 v31, v2
	v_mov_b32_e32 v32, v2
	v_mov_b32_e32 v33, v2
	v_and_b32_e32 v62, 63, v0
	v_lshrrev_b32_e32 v63, 2, v62
	v_and_b32_e32 v62, 3, v62
	v_sub_u32_e32 v64, 0, v1
	v_and_b32_e32 v64, 3, v64
	v_xor_b32_e32 v62, v62, v64
	v_lshlrev_b32_e32 v62, 4, v62
	v_lshl_or_b32 v62, v63, 11, v62
	s_lshl_b32 s13, s6, 4
	s_add_i32 s13, s13, s4
	s_lshl_b32 s13, s13, 11
	s_lshl_b32 s16, s6, 10
	s_add_i32 s16, s16, 0x2000
	s_waitcnt lgkmcnt(0)
	s_add_u32 s14, s14, s13
	s_addc_u32 s15, s15, 0
	s_add_i32 m0, s16, 0
	s_nop 0
	global_load_lds_dwordx4 v62, s[14:15] offset:0
	s_add_i32 m0, s16, 16320
	s_nop 0
	global_load_lds_dwordx4 v62, s[14:15] offset:64
	s_add_i32 m0, s16, 32640
	s_nop 0
	global_load_lds_dwordx4 v62, s[14:15] offset:128
	s_add_i32 m0, s16, 48960
	s_nop 0
	global_load_lds_dwordx4 v62, s[14:15] offset:192
	v_add_u32_e32 v62, 0x100, v62
	s_mov_b32 s17, 4
	.p2align	6
.Lg1_cloop:
	s_lshl_b32 s12, s8, 14
	v_add3_u32 v42, s12, v37, v35
	v_add3_u32 v58, s12, v36, v35
	s_waitcnt vmcnt(3)
	s_barrier
	ds_read_b128 v[38:41], v42 offset:8192
	ds_read_b128 v[42:45], v42 offset:9216
	ds_read_b128 v[46:49], v58
	ds_read_b128 v[50:53], v58 offset:1024
	ds_read_b128 v[54:57], v58 offset:2048
	ds_read_b128 v[58:61], v58 offset:3072
	s_lshl_b32 s13, s17, 14
	s_add_i32 m0, s13, s16
	s_add_i32 s13, s17, 1
	global_load_lds_dwordx4 v62, s[14:15]
	s_cmp_lg_u32 s17, 4
	s_cselect_b32 s17, s13, 0
	v_add_u32_e32 v62, 64, v62
	s_waitcnt lgkmcnt(0)
	v_mfma_f32_16x16x32_f16 v[30:33], v[46:49], v[38:41], v[30:33]
	s_add_i32 s12, s8, 1
	s_cmp_lg_u32 s8, 4
	s_cselect_b32 s8, s12, 0
	v_mfma_f32_16x16x32_f16 v[22:25], v[46:49], v[42:45], v[22:25]
	s_add_i32 s11, s11, -1
	s_cmp_eq_u32 s11, 0
	v_mfma_f32_16x16x32_f16 v[26:29], v[50:53], v[38:41], v[26:29]
	v_mfma_f32_16x16x32_f16 v[14:17], v[50:53], v[42:45], v[14:17]
	v_mfma_f32_16x16x32_f16 v[18:21], v[54:57], v[38:41], v[18:21]
	v_mfma_f32_16x16x32_f16 v[6:9], v[54:57], v[42:45], v[6:9]
	v_mfma_f32_16x16x32_f16 v[10:13], v[58:61], v[38:41], v[10:13]
	v_mfma_f32_16x16x32_f16 v[2:5], v[58:61], v[42:45], v[2:5]
	s_cbranch_scc0 .Lg1_cloop
	s_lshl_b32 s12, s8, 14
	v_add3_u32 v42, s12, v37, v35
	v_add3_u32 v58, s12, v36, v35
	s_waitcnt vmcnt(3)
	s_barrier
	ds_read_b128 v[38:41], v42 offset:8192
	ds_read_b128 v[42:45], v42 offset:9216
	ds_read_b128 v[46:49], v58
	ds_read_b128 v[50:53], v58 offset:1024
	ds_read_b128 v[54:57], v58 offset:2048
	ds_read_b128 v[58:61], v58 offset:3072
	s_waitcnt lgkmcnt(0)
	v_mfma_f32_16x16x32_f16 v[30:33], v[46:49], v[38:41], v[30:33]
	s_add_i32 s12, s8, 1
	s_cmp_lg_u32 s8, 4
	s_cselect_b32 s8, s12, 0
	v_mfma_f32_16x16x32_f16 v[22:25], v[46:49], v[42:45], v[22:25]
	v_mfma_f32_16x16x32_f16 v[26:29], v[50:53], v[38:41], v[26:29]
	v_mfma_f32_16x16x32_f16 v[14:17], v[50:53], v[42:45], v[14:17]
	v_mfma_f32_16x16x32_f16 v[18:21], v[54:57], v[38:41], v[18:21]
	v_mfma_f32_16x16x32_f16 v[6:9], v[54:57], v[42:45], v[6:9]
	v_mfma_f32_16x16x32_f16 v[10:13], v[58:61], v[38:41], v[10:13]
	v_mfma_f32_16x16x32_f16 v[2:5], v[58:61], v[42:45], v[2:5]
	s_lshl_b32 s12, s8, 14
	v_add3_u32 v42, s12, v37, v35
	v_add3_u32 v58, s12, v36, v35
	s_waitcnt vmcnt(2)
	s_barrier
	ds_read_b128 v[38:41], v42 offset:8192
	ds_read_b128 v[42:45], v42 offset:9216
	ds_read_b128 v[46:49], v58
	ds_read_b128 v[50:53], v58 offset:1024
	ds_read_b128 v[54:57], v58 offset:2048
	ds_read_b128 v[58:61], v58 offset:3072
	s_waitcnt lgkmcnt(0)
	v_mfma_f32_16x16x32_f16 v[30:33], v[46:49], v[38:41], v[30:33]
	s_add_i32 s12, s8, 1
	s_cmp_lg_u32 s8, 4
	s_cselect_b32 s8, s12, 0
	v_mfma_f32_16x16x32_f16 v[22:25], v[46:49], v[42:45], v[22:25]
	v_mfma_f32_16x16x32_f16 v[26:29], v[50:53], v[38:41], v[26:29]
	v_mfma_f32_16x16x32_f16 v[14:17], v[50:53], v[42:45], v[14:17]
	v_mfma_f32_16x16x32_f16 v[18:21], v[54:57], v[38:41], v[18:21]
	v_mfma_f32_16x16x32_f16 v[6:9], v[54:57], v[42:45], v[6:9]
	v_mfma_f32_16x16x32_f16 v[10:13], v[58:61], v[38:41], v[10:13]
	v_mfma_f32_16x16x32_f16 v[2:5], v[58:61], v[42:45], v[2:5]
	s_lshl_b32 s12, s8, 14
	v_add3_u32 v42, s12, v37, v35
	v_add3_u32 v58, s12, v36, v35
	s_waitcnt vmcnt(1)
	s_barrier
	ds_read_b128 v[38:41], v42 offset:8192
	ds_read_b128 v[42:45], v42 offset:9216
	ds_read_b128 v[46:49], v58
	ds_read_b128 v[50:53], v58 offset:1024
	ds_read_b128 v[54:57], v58 offset:2048
	ds_read_b128 v[58:61], v58 offset:3072
	s_waitcnt lgkmcnt(0)
	v_mfma_f32_16x16x32_f16 v[30:33], v[46:49], v[38:41], v[30:33]
	s_add_i32 s12, s8, 1
	s_cmp_lg_u32 s8, 4
	s_cselect_b32 s8, s12, 0
	v_mfma_f32_16x16x32_f16 v[22:25], v[46:49], v[42:45], v[22:25]
	v_mfma_f32_16x16x32_f16 v[26:29], v[50:53], v[38:41], v[26:29]
	v_mfma_f32_16x16x32_f16 v[14:17], v[50:53], v[42:45], v[14:17]
	v_mfma_f32_16x16x32_f16 v[18:21], v[54:57], v[38:41], v[18:21]
	v_mfma_f32_16x16x32_f16 v[6:9], v[54:57], v[42:45], v[6:9]
	v_mfma_f32_16x16x32_f16 v[10:13], v[58:61], v[38:41], v[10:13]
	v_mfma_f32_16x16x32_f16 v[2:5], v[58:61], v[42:45], v[2:5]
	s_lshl_b32 s12, s8, 14
	v_add3_u32 v42, s12, v37, v35
	v_add3_u32 v58, s12, v36, v35
	s_waitcnt vmcnt(0)
	s_barrier
	ds_read_b128 v[38:41], v42 offset:8192
	ds_read_b128 v[42:45], v42 offset:9216
	ds_read_b128 v[46:49], v58
	ds_read_b128 v[50:53], v58 offset:1024
	ds_read_b128 v[54:57], v58 offset:2048
	ds_read_b128 v[58:61], v58 offset:3072
	s_waitcnt lgkmcnt(0)
	v_mfma_f32_16x16x32_f16 v[30:33], v[46:49], v[38:41], v[30:33]
	s_add_i32 s12, s8, 1
	s_cmp_lg_u32 s8, 4
	s_cselect_b32 s8, s12, 0
	v_mfma_f32_16x16x32_f16 v[22:25], v[46:49], v[42:45], v[22:25]
	v_mfma_f32_16x16x32_f16 v[26:29], v[50:53], v[38:41], v[26:29]
	v_mfma_f32_16x16x32_f16 v[14:17], v[50:53], v[42:45], v[14:17]
	v_mfma_f32_16x16x32_f16 v[18:21], v[54:57], v[38:41], v[18:21]
	v_mfma_f32_16x16x32_f16 v[6:9], v[54:57], v[42:45], v[6:9]
	v_mfma_f32_16x16x32_f16 v[10:13], v[58:61], v[38:41], v[10:13]
	v_mfma_f32_16x16x32_f16 v[2:5], v[58:61], v[42:45], v[2:5]
	s_or_b32 s8, s10, s4
	v_or_b32_e32 v35, s8, v34
	v_lshl_or_b32 v34, v1, 2, s9
	v_mov_b32_e32 v37, 0
	v_or_b32_e32 v34, s7, v34
	v_lshlrev_b32_e32 v36, 12, v35
	v_mov_b32_e32 v35, v37
	v_lshl_add_u64 v[38:39], s[2:3], 0, v[36:37]
	v_lshlrev_b64 v[40:41], 2, v[34:35]
	v_lshl_add_u64 v[42:43], v[38:39], 0, v[40:41]
	s_mov_b64 s[2:3], 0x10000
	v_lshl_add_u64 v[44:45], v[42:43], 0, s[2:3]
	global_store_dwordx4 v[42:43], v[30:33], off sc1
	global_store_dwordx4 v[42:43], v[26:29], off offset:64 sc1
	global_store_dwordx4 v[42:43], v[18:21], off offset:128 sc1
	global_store_dwordx4 v[42:43], v[10:13], off offset:192 sc1
	global_store_dwordx4 v[44:45], v[22:25], off sc1
	global_store_dwordx4 v[44:45], v[14:17], off offset:64 sc1
	global_store_dwordx4 v[44:45], v[6:9], off offset:128 sc1
	global_store_dwordx4 v[44:45], v[2:5], off offset:192 sc1
	s_branch .LBB3_2
